# speedup vs baseline: 1.0100x; 1.0072x over previous
.Lno_pre:
	s_nop 15
	s_nop 3
	v_cvt_pk_f16_f32 v38, v64, v65
	v_cvt_pk_f16_f32 v39, v66, v67
	v_and_b32 v36, s35, v38
	v_and_b32 v37, s35, v39
	v_pk_fma_f16 v238, v36, s42, v227
	v_pk_fma_f16 v239, v37, s42, v227
	v_pk_fma_f16 v238, v238, v36, s43
	v_pk_fma_f16 v239, v239, v37, s43
	s_nop 0
	v_pk_mul_f16 v238, v238, v36
	v_pk_mul_f16 v239, v239, v37
	v_exp_f16_sdwa v238, v238 dst_sel:WORD_0 dst_unused:UNUSED_PRESERVE src0_sel:WORD_0
	v_exp_f16_sdwa v239, v239 dst_sel:WORD_0 dst_unused:UNUSED_PRESERVE src0_sel:WORD_0
	v_exp_f16_sdwa v238, v238 dst_sel:WORD_1 dst_unused:UNUSED_PRESERVE src0_sel:WORD_1
	v_exp_f16_sdwa v239, v239 dst_sel:WORD_1 dst_unused:UNUSED_PRESERVE src0_sel:WORD_1
	v_pk_add_f16 v40, v38, v36
	v_pk_add_f16 v41, v39, v37
	v_pk_fma_f16 v238, v36, v238, v40 neg_lo:[1,0,0] neg_hi:[1,0,0]
	v_pk_fma_f16 v239, v37, v239, v41 neg_lo:[1,0,0] neg_hi:[1,0,0]
	v_cvt_pk_f16_f32 v38, v68, v69
	v_cvt_pk_f16_f32 v39, v70, v71
	v_and_b32 v36, s35, v38
	v_and_b32 v37, s35, v39
	v_pk_fma_f16 v240, v36, s42, v227
	v_pk_fma_f16 v241, v37, s42, v227
	v_pk_fma_f16 v240, v240, v36, s43
	v_pk_fma_f16 v241, v241, v37, s43
	v_cvt_pk_f16_f32 v243, v72, v73
	v_cvt_pk_f16_f32 v244, v74, v75
	v_and_b32 v209, s35, v243
	v_and_b32 v242, s35, v244
	v_pk_fma_f16 v68, v209, s42, v227
	v_pk_fma_f16 v69, v242, s42, v227
	v_pk_fma_f16 v68, v68, v209, s43
	v_pk_fma_f16 v69, v69, v242, s43
	v_cvt_pk_f16_f32 v74, v76, v77
	v_cvt_pk_f16_f32 v75, v78, v79
	v_and_b32 v72, s35, v74
	v_and_b32 v73, s35, v75
	v_pk_fma_f16 v70, v72, s42, v227
	v_pk_fma_f16 v71, v73, s42, v227
	v_pk_fma_f16 v70, v70, v72, s43
	v_pk_fma_f16 v71, v71, v73, s43
	s_cmp_eq_u32 s8, 0
	v_pk_mul_f16 v240, v240, v36
	v_pk_mul_f16 v241, v241, v37
	v_exp_f16_sdwa v240, v240 dst_sel:WORD_0 dst_unused:UNUSED_PRESERVE src0_sel:WORD_0
	v_exp_f16_sdwa v241, v241 dst_sel:WORD_0 dst_unused:UNUSED_PRESERVE src0_sel:WORD_0
	v_exp_f16_sdwa v240, v240 dst_sel:WORD_1 dst_unused:UNUSED_PRESERVE src0_sel:WORD_1
	v_exp_f16_sdwa v241, v241 dst_sel:WORD_1 dst_unused:UNUSED_PRESERVE src0_sel:WORD_1
	v_pk_add_f16 v40, v38, v36
	v_pk_add_f16 v41, v39, v37
	v_pk_fma_f16 v240, v36, v240, v40 neg_lo:[1,0,0] neg_hi:[1,0,0]
	v_pk_fma_f16 v241, v37, v241, v41 neg_lo:[1,0,0] neg_hi:[1,0,0]
	v_pk_mul_f16 v68, v68, v209
	v_pk_mul_f16 v69, v69, v242
	v_exp_f16_sdwa v68, v68 dst_sel:WORD_0 dst_unused:UNUSED_PRESERVE src0_sel:WORD_0
	v_exp_f16_sdwa v69, v69 dst_sel:WORD_0 dst_unused:UNUSED_PRESERVE src0_sel:WORD_0
	v_exp_f16_sdwa v68, v68 dst_sel:WORD_1 dst_unused:UNUSED_PRESERVE src0_sel:WORD_1
	v_exp_f16_sdwa v69, v69 dst_sel:WORD_1 dst_unused:UNUSED_PRESERVE src0_sel:WORD_1
	v_pk_add_f16 v76, v243, v209
	v_pk_add_f16 v77, v244, v242
	v_pk_fma_f16 v68, v209, v68, v76 neg_lo:[1,0,0] neg_hi:[1,0,0]
	v_pk_fma_f16 v69, v242, v69, v77 neg_lo:[1,0,0] neg_hi:[1,0,0]
	v_pk_mul_f16 v70, v70, v72
	v_pk_mul_f16 v71, v71, v73
	v_exp_f16_sdwa v70, v70 dst_sel:WORD_0 dst_unused:UNUSED_PRESERVE src0_sel:WORD_0
	v_exp_f16_sdwa v71, v71 dst_sel:WORD_0 dst_unused:UNUSED_PRESERVE src0_sel:WORD_0
	v_exp_f16_sdwa v70, v70 dst_sel:WORD_1 dst_unused:UNUSED_PRESERVE src0_sel:WORD_1
	v_exp_f16_sdwa v71, v71 dst_sel:WORD_1 dst_unused:UNUSED_PRESERVE src0_sel:WORD_1
	v_pk_add_f16 v76, v74, v72
	v_pk_add_f16 v77, v75, v73
	v_pk_fma_f16 v70, v72, v70, v76 neg_lo:[1,0,0] neg_hi:[1,0,0]
	v_pk_fma_f16 v71, v73, v71, v77 neg_lo:[1,0,0] neg_hi:[1,0,0]
	v_cvt_pk_f16_f32 v74, v48, v49
	v_cvt_pk_f16_f32 v75, v50, v51
	v_and_b32 v72, s35, v74
	v_and_b32 v73, s35, v75
	v_pk_fma_f16 v64, v72, s42, v227
	v_pk_fma_f16 v65, v73, s42, v227
	v_pk_fma_f16 v64, v64, v72, s43
	v_pk_fma_f16 v65, v65, v73, s43
	v_cvt_pk_f16_f32 v78, v52, v53
	v_cvt_pk_f16_f32 v79, v54, v55
	v_and_b32 v76, s35, v78
	v_and_b32 v77, s35, v79
	v_pk_fma_f16 v66, v76, s42, v227
	v_pk_fma_f16 v67, v77, s42, v227
	v_pk_fma_f16 v66, v66, v76, s43
	v_pk_fma_f16 v67, v67, v77, s43
	v_pk_mul_f16 v64, v64, v72
	v_pk_mul_f16 v65, v65, v73
	v_exp_f16_sdwa v64, v64 dst_sel:WORD_0 dst_unused:UNUSED_PRESERVE src0_sel:WORD_0
	v_exp_f16_sdwa v65, v65 dst_sel:WORD_0 dst_unused:UNUSED_PRESERVE src0_sel:WORD_0
	v_exp_f16_sdwa v64, v64 dst_sel:WORD_1 dst_unused:UNUSED_PRESERVE src0_sel:WORD_1
	v_exp_f16_sdwa v65, v65 dst_sel:WORD_1 dst_unused:UNUSED_PRESERVE src0_sel:WORD_1
	v_pk_add_f16 v209, v74, v72
	v_pk_add_f16 v242, v75, v73
	v_pk_fma_f16 v64, v72, v64, v209 neg_lo:[1,0,0] neg_hi:[1,0,0]
	v_pk_fma_f16 v65, v73, v65, v242 neg_lo:[1,0,0] neg_hi:[1,0,0]
	v_pk_mul_f16 v66, v66, v76
	v_pk_mul_f16 v67, v67, v77
	v_exp_f16_sdwa v66, v66 dst_sel:WORD_0 dst_unused:UNUSED_PRESERVE src0_sel:WORD_0
	v_exp_f16_sdwa v67, v67 dst_sel:WORD_0 dst_unused:UNUSED_PRESERVE src0_sel:WORD_0
	v_exp_f16_sdwa v66, v66 dst_sel:WORD_1 dst_unused:UNUSED_PRESERVE src0_sel:WORD_1
	v_exp_f16_sdwa v67, v67 dst_sel:WORD_1 dst_unused:UNUSED_PRESERVE src0_sel:WORD_1
	v_pk_add_f16 v72, v78, v76
	v_pk_add_f16 v73, v79, v77
	v_pk_fma_f16 v66, v76, v66, v72 neg_lo:[1,0,0] neg_hi:[1,0,0]
	v_pk_fma_f16 v67, v77, v67, v73 neg_lo:[1,0,0] neg_hi:[1,0,0]
	v_cvt_pk_f16_f32 v74, v56, v57
	v_cvt_pk_f16_f32 v75, v58, v59
	v_and_b32 v72, s35, v74
	v_and_b32 v73, s35, v75
	v_pk_fma_f16 v48, v72, s42, v227
	v_pk_fma_f16 v49, v73, s42, v227
	v_pk_fma_f16 v48, v48, v72, s43
	v_pk_fma_f16 v49, v49, v73, s43
	v_cvt_pk_f16_f32 v58, v60, v61
	v_cvt_pk_f16_f32 v59, v62, v63
	v_and_b32 v56, s35, v58
	v_and_b32 v57, s35, v59
	v_pk_fma_f16 v50, v56, s42, v227
	v_pk_fma_f16 v51, v57, s42, v227
	v_pk_fma_f16 v50, v50, v56, s43
	v_pk_fma_f16 v51, v51, v57, s43
	v_pk_mul_f16 v48, v48, v72
	v_pk_mul_f16 v49, v49, v73
	v_exp_f16_sdwa v48, v48 dst_sel:WORD_0 dst_unused:UNUSED_PRESERVE src0_sel:WORD_0
	v_exp_f16_sdwa v49, v49 dst_sel:WORD_0 dst_unused:UNUSED_PRESERVE src0_sel:WORD_0
	v_exp_f16_sdwa v48, v48 dst_sel:WORD_1 dst_unused:UNUSED_PRESERVE src0_sel:WORD_1
	v_exp_f16_sdwa v49, v49 dst_sel:WORD_1 dst_unused:UNUSED_PRESERVE src0_sel:WORD_1
	v_pk_add_f16 v62, v74, v72
	v_pk_add_f16 v63, v75, v73
	v_pk_fma_f16 v48, v72, v48, v62 neg_lo:[1,0,0] neg_hi:[1,0,0]
	v_pk_fma_f16 v49, v73, v49, v63 neg_lo:[1,0,0] neg_hi:[1,0,0]
	v_pk_mul_f16 v50, v50, v56
	v_pk_mul_f16 v51, v51, v57
	v_exp_f16_sdwa v50, v50 dst_sel:WORD_0 dst_unused:UNUSED_PRESERVE src0_sel:WORD_0
	v_exp_f16_sdwa v51, v51 dst_sel:WORD_0 dst_unused:UNUSED_PRESERVE src0_sel:WORD_0
	v_exp_f16_sdwa v50, v50 dst_sel:WORD_1 dst_unused:UNUSED_PRESERVE src0_sel:WORD_1
	v_exp_f16_sdwa v51, v51 dst_sel:WORD_1 dst_unused:UNUSED_PRESERVE src0_sel:WORD_1
	v_pk_add_f16 v62, v58, v56
	v_pk_add_f16 v63, v59, v57
	v_pk_fma_f16 v50, v56, v50, v62 neg_lo:[1,0,0] neg_hi:[1,0,0]
	v_pk_fma_f16 v51, v57, v51, v63 neg_lo:[1,0,0] neg_hi:[1,0,0]
	ds_write2_b64 v246, v[238:239], v[240:241] offset0:136 offset1:138
	ds_write2_b64 v246, v[64:65], v[66:67] offset0:144 offset1:146
	ds_write2_b64 v246, v[68:69], v[70:71] offset0:140 offset1:142
	ds_write2_b64 v246, v[48:49], v[50:51] offset0:148 offset1:150
	ds_read2_b64 v[24:27], v249 offset1:1
	ds_read2_b64 v[28:31], v249 offset0:8 offset1:9
	ds_read2_b64 v[40:43], v250 offset1:1
	ds_read2_b64 v[44:47], v250 offset0:8 offset1:9
	s_waitcnt lgkmcnt(2)
	v_mfma_f32_16x16x32_f16 v[32:35], v[24:27], v[16:19], 0
	v_mfma_f32_16x16x32_f16 v[32:35], v[28:31], v[20:23], v[32:35]
	s_waitcnt lgkmcnt(0)
	v_mfma_f32_16x16x32_f16 v[36:39], v[40:43], v[16:19], 0
	v_mfma_f32_16x16x32_f16 v[36:39], v[44:47], v[20:23], v[36:39]
	s_nop 7
	v_max3_f32 v52, v32, v33, v34
	v_max3_f32 v52, v52, v35, v36
	v_max3_f32 v52, v52, v37, v38
	v_max_f32_e32 v52, v52, v39
	v_mov_b32_e32 v53, v52
	s_nop 1
	v_permlane16_swap_b32_e32 v52, v53
	s_nop 0
	v_max_f32_e32 v52, v52, v53
	v_mov_b32_e32 v53, v52
	s_nop 1
	v_permlane32_swap_b32_e32 v52, v53
	s_nop 0
	v_max_f32_e32 v48, v52, v53
	s_cbranch_scc1 .LBB0_23
	v_add_f32_e32 v49, 0x41000000, v237
	v_cmp_gt_f32_e32 vcc, v48, v49
	s_cbranch_vccz .LBB0_24
	v_max_f32_e32 v48, v48, v48
	v_max_f32_e32 v49, v237, v237
	v_max_f32_e32 v49, v49, v48
	v_sub_f32_e32 v48, v237, v49
	v_exp_f32_e32 v48, v48
	v_mov_b32_e32 v237, v49
	v_pk_mul_f32 v[14:15], v[48:49], v[14:15] op_sel_hi:[0,1]
	v_pk_mul_f32 v[12:13], v[48:49], v[12:13] op_sel_hi:[0,1]
	v_pk_mul_f32 v[10:11], v[48:49], v[10:11] op_sel_hi:[0,1]
	v_pk_mul_f32 v[8:9], v[48:49], v[8:9] op_sel_hi:[0,1]
	v_pk_mul_f32 v[6:7], v[48:49], v[6:7] op_sel_hi:[0,1]
	v_pk_mul_f32 v[4:5], v[48:49], v[4:5] op_sel_hi:[0,1]
	v_pk_mul_f32 v[2:3], v[48:49], v[2:3] op_sel_hi:[0,1]
	v_pk_mul_f32 v[0:1], v[48:49], v[0:1] op_sel_hi:[0,1]
	v_mul_f32_e32 v236, v236, v48
	s_branch .LBB0_24
